# speedup vs baseline: 1.0219x; 1.0219x over previous
.LBB1_89:
	s_or_b64 exec, exec, s[18:19]
	s_barrier
	s_add_u32 s4, s0, s40
	s_addc_u32 s5, s1, s41
	v_and_b32_e32 v101, 48, v179
	v_lshlrev_b32_e32 v101, 4, v101
	v_and_b32_e32 v126, 7, v179
	v_lshl_or_b32 v101, v126, 10, v101
	v_bfe_u32 v126, v179, 3, 1
	v_lshl_or_b32 v101, v126, 17, v101
	v_add_u32_e32 v101, s90, v101
	s_add_u32 s0, s0, s42
	s_addc_u32 s1, s1, s43
	global_load_dwordx4 v[150:153], v101, s[4:5]
	global_load_dwordx4 v[138:141], v108, s[0:1]
	global_load_dwordx4 v[142:145], v108, s[0:1] offset:1024
	global_load_dwordx4 v[146:149], v108, s[0:1] offset:2048
	global_load_dwordx4 v[126:129], v108, s[0:1] offset:3072
	v_add_u32_e32 v100, s95, v108
	v_add_u32_e32 v98, s10, v108
	ds_read_b128 v[224:227], v100
	ds_read_b128 v[228:231], v98
	ds_read_b128 v[232:235], v100 offset:1024
	ds_read_b128 v[236:239], v98 offset:1024
	s_andn2_b64 vcc, exec, s[38:39]
	s_waitcnt vmcnt(4)
	v_mov_b32_dpp v174, v150 row_shl:8 row_mask:0xf bank_mask:0xf bound_ctrl:1
	v_mov_b32_dpp v175, v151 row_shl:8 row_mask:0xf bank_mask:0xf bound_ctrl:1
	v_mov_b32_dpp v176, v152 row_shl:8 row_mask:0xf bank_mask:0xf bound_ctrl:1
	v_mov_b32_dpp v177, v153 row_shl:8 row_mask:0xf bank_mask:0xf bound_ctrl:1
	v_mov_b32_dpp v196, v150 row_shl:1 row_mask:0xf bank_mask:0xf bound_ctrl:1
	v_mov_b32_dpp v197, v151 row_shl:1 row_mask:0xf bank_mask:0xf bound_ctrl:1
	v_mov_b32_dpp v198, v152 row_shl:1 row_mask:0xf bank_mask:0xf bound_ctrl:1
	v_mov_b32_dpp v199, v153 row_shl:1 row_mask:0xf bank_mask:0xf bound_ctrl:1
	v_mov_b32_dpp v200, v150 row_shl:9 row_mask:0xf bank_mask:0xf bound_ctrl:1
	v_mov_b32_dpp v201, v151 row_shl:9 row_mask:0xf bank_mask:0xf bound_ctrl:1
	v_mov_b32_dpp v202, v152 row_shl:9 row_mask:0xf bank_mask:0xf bound_ctrl:1
	v_mov_b32_dpp v203, v153 row_shl:9 row_mask:0xf bank_mask:0xf bound_ctrl:1
	s_waitcnt lgkmcnt(2)
	v_mfma_f32_16x16x32_f16 v[204:207], v[224:227], v[150:153], 0
	v_mfma_f32_16x16x32_f16 v[212:215], v[228:231], v[150:153], 0
	v_mfma_f32_16x16x32_f16 v[216:219], v[224:227], v[174:177], 0
	ds_read_b128 v[224:227], v100 offset:2048
	ds_read_b128 v[228:231], v98 offset:2048
	v_mov_b32_dpp v154, v150 row_shl:2 row_mask:0xf bank_mask:0xf bound_ctrl:1
	v_mov_b32_dpp v155, v151 row_shl:2 row_mask:0xf bank_mask:0xf bound_ctrl:1
	v_mov_b32_dpp v156, v152 row_shl:2 row_mask:0xf bank_mask:0xf bound_ctrl:1
	v_mov_b32_dpp v157, v153 row_shl:2 row_mask:0xf bank_mask:0xf bound_ctrl:1
	v_mov_b32_dpp v174, v150 row_shl:10 row_mask:0xf bank_mask:0xf bound_ctrl:1
	v_mov_b32_dpp v175, v151 row_shl:10 row_mask:0xf bank_mask:0xf bound_ctrl:1
	v_mov_b32_dpp v176, v152 row_shl:10 row_mask:0xf bank_mask:0xf bound_ctrl:1
	v_mov_b32_dpp v177, v153 row_shl:10 row_mask:0xf bank_mask:0xf bound_ctrl:1
	s_waitcnt lgkmcnt(2)
	v_mfma_f32_16x16x32_f16 v[208:211], v[232:235], v[196:199], 0
	v_mfma_f32_16x16x32_f16 v[220:223], v[236:239], v[196:199], 0
	v_mfma_f32_16x16x32_f16 v[134:137], v[232:235], v[200:203], 0
	ds_read_b128 v[232:235], v100 offset:3072
	ds_read_b128 v[236:239], v98 offset:3072
	v_mov_b32_dpp v196, v150 row_shl:3 row_mask:0xf bank_mask:0xf bound_ctrl:1
	v_mov_b32_dpp v197, v151 row_shl:3 row_mask:0xf bank_mask:0xf bound_ctrl:1
	v_mov_b32_dpp v198, v152 row_shl:3 row_mask:0xf bank_mask:0xf bound_ctrl:1
	v_mov_b32_dpp v199, v153 row_shl:3 row_mask:0xf bank_mask:0xf bound_ctrl:1
	v_mov_b32_dpp v200, v150 row_shl:11 row_mask:0xf bank_mask:0xf bound_ctrl:1
	v_mov_b32_dpp v201, v151 row_shl:11 row_mask:0xf bank_mask:0xf bound_ctrl:1
	v_mov_b32_dpp v202, v152 row_shl:11 row_mask:0xf bank_mask:0xf bound_ctrl:1
	v_mov_b32_dpp v203, v153 row_shl:11 row_mask:0xf bank_mask:0xf bound_ctrl:1
	s_waitcnt lgkmcnt(2)
	v_mfma_f32_16x16x32_f16 v[204:207], v[224:227], v[154:157], v[204:207]
	v_mfma_f32_16x16x32_f16 v[212:215], v[228:231], v[154:157], v[212:215]
	v_mfma_f32_16x16x32_f16 v[216:219], v[224:227], v[174:177], v[216:219]
	ds_read_b128 v[224:227], v100 offset:4096
	ds_read_b128 v[228:231], v98 offset:4096
	v_mov_b32_dpp v154, v150 row_shl:4 row_mask:0xf bank_mask:0xf bound_ctrl:1
	v_mov_b32_dpp v155, v151 row_shl:4 row_mask:0xf bank_mask:0xf bound_ctrl:1
	v_mov_b32_dpp v156, v152 row_shl:4 row_mask:0xf bank_mask:0xf bound_ctrl:1
	v_mov_b32_dpp v157, v153 row_shl:4 row_mask:0xf bank_mask:0xf bound_ctrl:1
	v_mov_b32_dpp v174, v150 row_shl:12 row_mask:0xf bank_mask:0xf bound_ctrl:1
	v_mov_b32_dpp v175, v151 row_shl:12 row_mask:0xf bank_mask:0xf bound_ctrl:1
	v_mov_b32_dpp v176, v152 row_shl:12 row_mask:0xf bank_mask:0xf bound_ctrl:1
	v_mov_b32_dpp v177, v153 row_shl:12 row_mask:0xf bank_mask:0xf bound_ctrl:1
	s_waitcnt lgkmcnt(2)
	v_mfma_f32_16x16x32_f16 v[208:211], v[232:235], v[196:199], v[208:211]
	v_mfma_f32_16x16x32_f16 v[220:223], v[236:239], v[196:199], v[220:223]
	v_mfma_f32_16x16x32_f16 v[134:137], v[232:235], v[200:203], v[134:137]
	ds_read_b128 v[232:235], v100 offset:5120
	ds_read_b128 v[236:239], v98 offset:5120
	v_mov_b32_dpp v196, v150 row_shl:5 row_mask:0xf bank_mask:0xf bound_ctrl:1
	v_mov_b32_dpp v197, v151 row_shl:5 row_mask:0xf bank_mask:0xf bound_ctrl:1
	v_mov_b32_dpp v198, v152 row_shl:5 row_mask:0xf bank_mask:0xf bound_ctrl:1
	v_mov_b32_dpp v199, v153 row_shl:5 row_mask:0xf bank_mask:0xf bound_ctrl:1
	v_mov_b32_dpp v200, v150 row_shl:13 row_mask:0xf bank_mask:0xf bound_ctrl:1
	v_mov_b32_dpp v201, v151 row_shl:13 row_mask:0xf bank_mask:0xf bound_ctrl:1
	v_mov_b32_dpp v202, v152 row_shl:13 row_mask:0xf bank_mask:0xf bound_ctrl:1
	v_mov_b32_dpp v203, v153 row_shl:13 row_mask:0xf bank_mask:0xf bound_ctrl:1
	s_waitcnt lgkmcnt(2)
	v_mfma_f32_16x16x32_f16 v[204:207], v[224:227], v[154:157], v[204:207]
	v_mfma_f32_16x16x32_f16 v[212:215], v[228:231], v[154:157], v[212:215]
	v_mfma_f32_16x16x32_f16 v[216:219], v[224:227], v[174:177], v[216:219]
	ds_read_b128 v[224:227], v100 offset:6144
	ds_read_b128 v[228:231], v98 offset:6144
	v_mov_b32_dpp v154, v150 row_shl:6 row_mask:0xf bank_mask:0xf bound_ctrl:1
	v_mov_b32_dpp v155, v151 row_shl:6 row_mask:0xf bank_mask:0xf bound_ctrl:1
	v_mov_b32_dpp v156, v152 row_shl:6 row_mask:0xf bank_mask:0xf bound_ctrl:1
	v_mov_b32_dpp v157, v153 row_shl:6 row_mask:0xf bank_mask:0xf bound_ctrl:1
	v_mov_b32_dpp v174, v150 row_shl:14 row_mask:0xf bank_mask:0xf bound_ctrl:1
	v_mov_b32_dpp v175, v151 row_shl:14 row_mask:0xf bank_mask:0xf bound_ctrl:1
	v_mov_b32_dpp v176, v152 row_shl:14 row_mask:0xf bank_mask:0xf bound_ctrl:1
	v_mov_b32_dpp v177, v153 row_shl:14 row_mask:0xf bank_mask:0xf bound_ctrl:1
	s_waitcnt lgkmcnt(2)
	v_mfma_f32_16x16x32_f16 v[208:211], v[232:235], v[196:199], v[208:211]
	v_mfma_f32_16x16x32_f16 v[220:223], v[236:239], v[196:199], v[220:223]
	v_mfma_f32_16x16x32_f16 v[134:137], v[232:235], v[200:203], v[134:137]
	ds_read_b128 v[232:235], v100 offset:7168
	s_cbranch_vccnz .Lc1_skip_afl7
	ds_read_b128 v[110:113], v98 offset:7168
.Lc1_skip_afl7:
	v_mov_b32_dpp v196, v150 row_shl:7 row_mask:0xf bank_mask:0xf bound_ctrl:1
	v_mov_b32_dpp v197, v151 row_shl:7 row_mask:0xf bank_mask:0xf bound_ctrl:1
	v_mov_b32_dpp v198, v152 row_shl:7 row_mask:0xf bank_mask:0xf bound_ctrl:1
	v_mov_b32_dpp v199, v153 row_shl:7 row_mask:0xf bank_mask:0xf bound_ctrl:1
	v_mov_b32_dpp v200, v150 row_shl:15 row_mask:0xf bank_mask:0xf bound_ctrl:1
	v_mov_b32_dpp v201, v151 row_shl:15 row_mask:0xf bank_mask:0xf bound_ctrl:1
	v_mov_b32_dpp v202, v152 row_shl:15 row_mask:0xf bank_mask:0xf bound_ctrl:1
	v_mov_b32_dpp v203, v153 row_shl:15 row_mask:0xf bank_mask:0xf bound_ctrl:1
	s_waitcnt lgkmcnt(1)
	v_mfma_f32_16x16x32_f16 v[162:165], v[224:227], v[154:157], v[204:207]
	v_mfma_f32_16x16x32_f16 v[166:169], v[228:231], v[154:157], v[212:215]
	v_mfma_f32_16x16x32_f16 v[170:173], v[224:227], v[174:177], v[216:219]
	s_waitcnt lgkmcnt(0)
	v_mfma_f32_16x16x32_f16 v[158:161], v[232:235], v[196:199], v[208:211]
	v_mfma_f32_16x16x32_f16 v[130:133], v[110:113], v[196:199], v[220:223]
	v_mfma_f32_16x16x32_f16 v[110:113], v[232:235], v[200:203], v[134:137]
	s_waitcnt vmcnt(3)
	v_mfma_f32_16x16x32_f16 v[114:117], v[114:117], v[138:141], 0
	v_and_b32_e32 v98, 15, v179
	v_cmp_eq_u32_e32 vcc, 0, v98
	s_waitcnt vmcnt(2)
	v_mfma_f32_16x16x32_f16 v[114:117], v[118:121], v[142:145], v[114:117]
	s_waitcnt vmcnt(1)
	v_mfma_f32_16x16x32_f16 v[114:117], v[122:125], v[146:149], v[114:117]
	s_waitcnt vmcnt(0)
	v_mfma_f32_16x16x32_f16 v[104:107], v[104:107], v[126:129], v[114:117]
	s_nop 7
	s_and_saveexec_b64 s[0:1], vcc
	s_cbranch_execz .LBB1_93
	v_pk_add_f32 v[100:101], v[172:173], v[168:169]
	v_pk_add_f32 v[114:115], v[170:171], v[166:167]
	s_nop 0
	v_pk_add_f32 v[100:101], v[132:133], v[100:101]
	v_pk_add_f32 v[114:115], v[130:131], v[114:115]
	v_pk_add_f32 v[100:101], v[112:113], v[100:101]
	v_pk_add_f32 v[110:111], v[110:111], v[114:115]
	v_readlane_b32 s4, v240, 17
	v_pk_fma_f32 v[110:111], v[110:111], s[92:93], v[158:159] op_sel_hi:[1,0,1]
	v_pk_fma_f32 v[100:101], v[100:101], s[92:93], v[160:161] op_sel_hi:[1,0,1]
	v_add_u32_e32 v108, s4, v103
	v_pk_add_f32 v[110:111], v[162:163], v[110:111]
	v_pk_add_f32 v[100:101], v[164:165], v[100:101]
	ds_write2_b32 v108, v110, v111 offset1:1
	ds_write2_b32 v108, v100, v101 offset0:2 offset1:3
